# speedup vs baseline: 1.0044x; 1.0044x over previous
_Z12fused_kernel6Params:
	s_load_dwordx16 s[52:67], s[0:1], 0x0
	s_load_dwordx16 s[36:51], s[0:1], 0x40
	s_load_dwordx16 s[8:23], s[0:1], 0x80
	s_load_dwordx4 s[24:27], s[0:1], 0xc0
	s_and_b32 s3, s2, 0x7f
	s_cmpk_gt_u32 s2, 0x7f
	v_and_b32_e32 v80, 63, v0
	s_mov_b64 s[0:1], -1
	s_mul_i32 s33, s3, 0x1c20
	s_cbranch_scc0 .Lk_217
	s_sleep 112
	v_readfirstlane_b32 s4, v0
	s_cmpk_lt_u32 s4, 0x300
	s_cbranch_scc1 .Lk_3
	s_setprio 1
